# P0 fp8 weight (W8) stores with sc1 (write-through)
# speedup vs baseline: 1.0075x; 1.0075x over previous
.LBB0_16:
	v_readfirstlane_b32 s50, v18
	s_lshl_b32 s51, s8, 12
	s_lshl_b32 s50, s50, 2
	s_add_u32 s50, s50, s51
	s_add_u32 s56, s6, s50
	s_addc_u32 s57, s7, 0
	v_and_b32_e32 v100, 3, v36
	v_lshrrev_b32_e32 v101, 5, v36
	v_lshl_or_b32 v100, v101, 2, v100
	v_bfe_u32 v101, v36, 2, 3
	v_lshlrev_b32_e32 v102, 12, v100
	v_lshl_or_b32 v102, v101, 4, v102
	v_lshlrev_b32_e32 v103, 2, v6
	v_sub_u32_e32 v103, v8, v103
	v_mad_u32_u24 v103, v100, s15, v103
	v_lshl_add_u32 v103, v101, 4, v103
	global_load_dwordx4 v[120:123], v102, s[56:57] nt
	s_add_u32 s56, s56, 0x8000
	s_addc_u32 s57, s57, 0
	global_load_dwordx4 v[124:127], v102, s[56:57] nt
	s_add_u32 s56, s56, 0x8000
	s_addc_u32 s57, s57, 0
	s_cmp_lg_u32 s60, 0
	s_cbranch_scc0 .Lnp_dn
	global_store_dwordx4 v[164:165], v[160:163], off sc1
	global_store_dwordx4 v[170:171], v[166:169], off sc1
	s_waitcnt vmcnt(2)
	s_branch .Ljoin_dn

.Lks_done:
	global_load_dwordx4 v[120:123], v102, s[56:57] nt
	s_add_u32 s56, s56, 0x10000
	s_addc_u32 s57, s57, 0
	global_load_dwordx4 v[124:127], v102, s[56:57] nt
	s_add_u32 s56, s56, 0x10000
	s_addc_u32 s57, s57, 0
	s_cmp_lg_u32 s60, 0
	s_cbranch_scc0 .Lnp_gu
	global_store_dwordx4 v[164:165], v[160:163], off sc1
	global_store_dwordx4 v[170:171], v[166:169], off sc1
	s_waitcnt vmcnt(2)
	s_branch .Ljoin_gu

.LBB0_31:
	s_cmp_lg_u32 s60, 0
	s_cbranch_scc0 .Lnoflush
	global_store_dwordx4 v[164:165], v[160:163], off sc1
	global_store_dwordx4 v[170:171], v[166:169], off sc1
